# MLA: row-sum MFMA reads its fp8 ones rows from v210-v217 kept for the whole loop (no per-step re-materialization), on top of the spread exp2 schedule
# speedup vs baseline: 1.0126x; 1.0064x over previous
; #define WAITV(n) asm volatile("s_waitcnt vmcnt(%0)" ::"n"(n) : "memory")
; #define SBAR() do { asm volatile("s_waitcnt lgkmcnt(0)" ::: "memory"); __builtin_amdgcn_s_barrier(); asm volatile("" ::: "memory"); } while (0)
; DEV int otid() { int t = threadIdx.x; asm volatile("" : "+v"(t)); return t; }
; DEV unsigned char* ows_(unsigned char* w) { gptr_t g = (gptr_t)w; asm volatile("" : "+s"(g)); return (unsigned char*)g; }
; DEV unsigned lds_addr(LAS char* p) { return (unsigned)(uintptr_t)p; }
; #define MLA_ISSUE(t_, st_) do { const unsigned char* s_ = imgs + (size_t)(t_) * MLA_IMG + wid * (STG / 8) + lane * 16; const unsigned d_ = ldsw + (unsigned)((st_) * STG); \
;     _Pragma("unroll") for (int i_ = 0; i_ < STG / 8192; ++i_) glds16a(s_ + i_ * 1024, d_ + i_ * 1024); } while (0)
; template <int VAR> DEV void mla_unit(const Params& p, int layer, int b, int hd, int tokbase, int t0, int t1, LAS char* lds, SideJob& sj) {
;     unsigned char* ws = ows_(p.ws); const int tid = otid(), lane = tid & 63, wid = tid >> 6, r = lane & 31, h = lane >> 5;
;     constexpr int STG = MLA_IMG;
;     const float cinit = 15.0f - ((const float*)(ws + WS_SCAL))[layer * 8 + 1];
;     const int tok = tokbase + 32 * wid + r;
;     v8i qf[2];
; #pragma unroll
;     for (int sx = 0; sx < 2; ++sx) { const u32x4* q8 = (const u32x4*)(ws + WS_QC + (size_t)tok * 768 + hd * 128 + 64 * sx + 32 * h); const u32x4 a = q8[0], bq = q8[1];
;         qf[sx] = (v8i){(int)a[0], (int)a[1], (int)a[2], (int)a[3], (int)bq[0], (int)bq[1], (int)bq[2], (int)bq[3]}; }
;     const unsigned char* imgs = ws + WS_KVC + (size_t)((b * 6 + hd) * 130) * MLA_IMG;
;     const unsigned ldsw = (unsigned)__builtin_amdgcn_readfirstlane((int)(lds_addr(lds) + (unsigned)(wid * (STG / 8))));
;     ...
;     f32x16 cini, sA0, sA1, sB0, sB1, o0, o1, lacc;
; #pragma unroll
;     for (int i = 0; i < 16; ++i) { cini[i] = cinit; o0[i] = 0.f; o1[i] = 0.f; lacc[i] = 0.f; }
;     const unsigned koffl = (unsigned)(2 * h * 1024 + r * 16);
;     const unsigned voffl = (unsigned)MLA_VOFF + (unsigned)(2 * h * 1024 + r * 16);
;     const int ns = t1 - t0;
;     MLA_ISSUE(t0, 0);
;     WAITV(0); SBAR();
.LBB0_808:
	s_and_b64 vcc, exec, s[6:7]
	s_cbranch_vccz .LBB0_749
	s_ashr_i32 s2, s64, 6
	s_mul_hi_i32 s3, s2, 0x2aaaaaab
	s_lshr_b32 s6, s3, 31
	s_add_i32 s3, s3, s6
	s_mul_i32 s6, s3, 6
	s_sub_i32 s37, s2, s6
	s_lshl_b32 s6, s64, 8
	s_lshl_b32 s3, s3, 14
	s_and_b32 s6, s6, 0x3f00
	s_or_b32 s3, s3, s6
	s_mov_b64 s[6:7], s[38:39]
	v_mov_b32_e32 v52, v246
	s_lshl_b64 s[8:9], s[48:49], 2
	v_and_b32_e32 v7, 31, v52
	v_ashrrev_i32_e32 v6, 6, v52
	s_add_u32 s8, s6, s8
	v_or_b32_e32 v2, s3, v7
	s_addc_u32 s9, s7, s9
	v_lshl_add_u32 v180, v6, 5, v2
	v_mov_b64_e32 v[2:3], s[6:7]
	s_movk_i32 s3, 0x300
	global_load_dword v8, v247, s[8:9] offset:4
	v_mad_i64_i32 v[2:3], s[8:9], v180, s3, v[2:3]
	s_lshl_b32 s8, s37, 7
	s_ashr_i32 s9, s8, 31
	v_lshl_add_u64 v[2:3], v[2:3], 0, s[8:9]
	v_and_b32_e32 v178, 32, v52
	v_lshl_add_u64 v[2:3], v[2:3], 0, v[178:179]
	s_mov_b64 s[8:9], 0x33370100
	s_mov_b32 s3, 0x33370000
	v_lshl_add_u64 v[4:5], v[2:3], 0, s[8:9]
	v_add_co_u32_e32 v2, vcc, s3, v2
	s_mul_i32 s3, s2, 0x82
	s_nop 0
	v_addc_co_u32_e32 v3, vcc, 0, v3, vcc
	global_load_dwordx4 v[138:141], v[2:3], off offset:256
	global_load_dwordx4 v[142:145], v[4:5], off offset:16
	global_load_dwordx4 v[134:137], v[4:5], off offset:80
	global_load_dwordx4 v[130:133], v[4:5], off offset:64
	s_mul_i32 s8, s2, 0x30c000
	s_movk_i32 s2, 0xc00
	s_mul_hi_i32 s9, s3, 0x6000
	v_mul_lo_u32 v50, v6, s2
	s_add_u32 s20, s6, s8
	v_and_b32_e32 v3, 63, v52
	v_bfe_u32 v198, v52, 5, 1
	s_addc_u32 s21, s7, s9
	v_lshlrev_b32_e32 v4, 4, v7
	v_ashrrev_i32_e32 v51, 31, v50
	v_lshl_or_b32 v199, v198, 11, v4
	v_lshl_add_u64 v[4:5], s[20:21], 0, v[50:51]
	v_lshlrev_b32_e32 v178, 4, v3
	v_readfirstlane_b32 s60, v50
	v_lshl_add_u64 v[18:19], v[4:5], 0, v[178:179]
	s_mov_b64 s[20:21], 0x35800100
	s_add_i32 s60, s60, 0
	v_lshl_add_u64 v[4:5], v[18:19], 0, s[20:21]
	s_mov_b32 s2, m0
	s_mov_b32 m0, s60
	s_nop 0
	global_load_lds_dwordx4 v[4:5], off
	s_mov_b32 m0, s2
	s_mov_b64 s[20:21], 0x35800500
	v_lshl_add_u64 v[4:5], v[18:19], 0, s[20:21]
	s_add_i32 s2, s60, 0x400
	s_mov_b32 s3, m0
	s_mov_b32 m0, s2
	s_nop 0
	global_load_lds_dwordx4 v[4:5], off
	s_mov_b32 m0, s3
	s_mov_b64 s[20:21], 0x35800900
	v_lshl_add_u64 v[4:5], v[18:19], 0, s[20:21]
	s_add_i32 s2, s60, 0x800
	s_mov_b32 s3, m0
	s_mov_b32 m0, s2
	s_nop 0
	global_load_lds_dwordx4 v[4:5], off
	s_mov_b32 m0, s3
	s_waitcnt vmcnt(0)
	s_waitcnt lgkmcnt(0)
	s_barrier
; #define LAS __attribute__((address_space(3)))
; #define WAITV(n) asm volatile("s_waitcnt vmcnt(%0)" ::"n"(n) : "memory")
; #define SBAR() do { asm volatile("s_waitcnt lgkmcnt(0)" ::: "memory"); __builtin_amdgcn_s_barrier(); asm volatile("" ::: "memory"); } while (0)
; DEV float ex2(float x) { return __builtin_amdgcn_exp2f(x); }
; #define MFMA8(a, b, c) __builtin_amdgcn_mfma_scale_f32_32x32x64_f8f6f4((a), (b), (c), 0, 0, 0, 0x7f7f7f7f, 0, 0x7c7c7c7c)
; #define MLA_ISSUE(t_, st_) do { const unsigned char* s_ = imgs + (size_t)(t_) * MLA_IMG + wid * (STG / 8) + lane * 16; const unsigned d_ = ldsw + (unsigned)((st_) * STG); \
;     _Pragma("unroll") for (int i_ = 0; i_ < STG / 8192; ++i_) glds16a(s_ + i_ * 1024, d_ + i_ * 1024); } while (0)
; template <int VAR> DEV void mla_step(f32x16& C0, f32x16& C1, f32x16& P0, f32x16& P1, f32x16& o0, f32x16& o1, f32x16& lacc,
;                   const v8i (&qf)[2], const f32x16& cini, LAS char* kp, LAS char* vp, v8i& pw) {
;     ...
;     const v8i ones8 = {0x38383838, 0x38383838, 0x38383838, 0x38383838, 0x38383838, 0x38383838, 0x38383838, 0x38383838};
; template <int VAR> DEV void mla_unit(const Params& p, int layer, int b, int hd, int tokbase, int t0, int t1, LAS char* lds, SideJob& sj) {
;     ...
;     f32x16 cini, sA0, sA1, sB0, sB1, o0, o1, lacc;
; #pragma unroll
;     for (int i = 0; i < 16; ++i) { cini[i] = cinit; o0[i] = 0.f; o1[i] = 0.f; lacc[i] = 0.f; }
;     const unsigned koffl = (unsigned)(2 * h * 1024 + r * 16);
;     const unsigned voffl = (unsigned)MLA_VOFF + (unsigned)(2 * h * 1024 + r * 16);
;     const int ns = t1 - t0;
;     MLA_ISSUE(t0, 0);
;     WAITV(0); SBAR();
;     if (ns > 1) MLA_ISSUE(t0 + 1, 1);
;     { LAS char* kp = lds + koffl;
;       sA0 = MFMA8(mla_kf8(kp, 0, 0), qf[0], cini); sA1 = MFMA8(mla_kf8(kp, 1, 0), qf[0], cini);
;       sA0 = MFMA8(mla_kf8(kp, 0, 1), qf[1], sA0); sA1 = MFMA8(mla_kf8(kp, 1, 1), qf[1], sA1);
; #pragma unroll
;       for (int i = 0; i < 16; ++i) { sA0[i] = ex2(sA0[i]); sA1[i] = ex2(sA1[i]); } }
;     int slot = 0;
;     v8i pw = {0, 0, 0, 0, 0, 0, 0, 0};
	s_mov_b64 s[20:21], 0x35806100
	v_lshl_add_u64 v[20:21], v[18:19], 0, s[20:21]
	s_add_i32 s2, s60, 0x6000
	s_mov_b32 s3, m0
	s_mov_b32 m0, s2
	s_nop 0
	global_load_lds_dwordx4 v[20:21], off
	s_mov_b32 m0, s3
	s_mov_b64 s[20:21], 0x35806500
	v_lshl_add_u64 v[20:21], v[18:19], 0, s[20:21]
	s_add_i32 s2, s60, 0x6400
	s_mov_b32 s3, m0
	s_mov_b32 m0, s2
	s_nop 0
	global_load_lds_dwordx4 v[20:21], off
	s_mov_b32 m0, s3
	s_mov_b64 s[20:21], 0x35806900
	v_lshl_add_u64 v[18:19], v[18:19], 0, s[20:21]
	s_add_i32 s2, s60, 0x6800
	s_mov_b32 s3, m0
	s_mov_b32 m0, s2
	s_nop 0
	global_load_lds_dwordx4 v[18:19], off
	s_mov_b32 m0, s3
	v_add_u32_e32 v200, 0, v199
	ds_read_b128 v[18:21], v200
	ds_read_b128 v[22:25], v200 offset:1024
	s_waitcnt vmcnt(0)
	v_ashrrev_i32_e32 v191, 4, v52
	s_movk_i32 s2, 0x104
	v_ashrrev_i32_e32 v195, 3, v52
	v_ashrrev_i32_e32 v181, 31, v180
	s_mov_b32 s62, 0
	v_mov_b32_e32 v193, v179
	v_mov_b32_e32 v146, 0
	v_mov_b32_e32 v147, 0
	v_mov_b32_e32 v148, 0
	v_mov_b32_e32 v149, 0
	v_mov_b32_e32 v150, 0
	v_mov_b32_e32 v151, 0
	v_mov_b32_e32 v152, 0
	v_mov_b32_e32 v153, 0
	s_mov_b32 s61, 0
	v_sub_f32_e32 v2, 0x41700000, v8
	v_mov_b32_e32 v3, v2
	v_mov_b32_e32 v4, v2
	v_mov_b32_e32 v5, v2
	v_mov_b32_e32 v6, v2
	v_mov_b32_e32 v7, v2
	v_mov_b32_e32 v8, v2
	v_mov_b32_e32 v9, v2
	v_mov_b32_e32 v10, v2
	v_mov_b32_e32 v11, v2
	v_mov_b32_e32 v12, v2
	v_mov_b32_e32 v13, v2
	v_mov_b32_e32 v14, v2
	v_mov_b32_e32 v15, v2
	v_mov_b32_e32 v16, v2
	v_mov_b32_e32 v17, v2
	s_waitcnt lgkmcnt(0)
	s_nop 0
	v_mfma_scale_f32_32x32x64_f8f6f4 v[18:33], v[18:25], v[138:145], v[2:17], v209, v208 op_sel_hi:[0,0,0]
	ds_read_b128 v[34:37], v200 offset:512
	ds_read_b128 v[38:41], v200 offset:1536
	s_waitcnt lgkmcnt(0)
	v_mfma_scale_f32_32x32x64_f8f6f4 v[34:49], v[34:41], v[138:145], v[2:17], v209, v208 op_sel_hi:[0,0,0]
	ds_read_b128 v[54:57], v200 offset:4096
	ds_read_b128 v[58:61], v200 offset:5120
	s_waitcnt lgkmcnt(0)
	v_mfma_scale_f32_32x32x64_f8f6f4 v[18:33], v[54:61], v[130:137], v[18:33], v209, v208 op_sel_hi:[0,0,0]
	ds_read_b128 v[54:57], v200 offset:4608
	ds_read_b128 v[58:61], v200 offset:5632
	s_waitcnt lgkmcnt(0)
	v_mfma_scale_f32_32x32x64_f8f6f4 v[34:49], v[54:61], v[130:137], v[34:49], v209, v208 op_sel_hi:[0,0,0]
	s_nop 15
	v_exp_f32_e32 v82, v18
	v_lshlrev_b32_e32 v18, 2, v52
	v_and_b32_e32 v190, 60, v18
	v_exp_f32_e32 v83, v19
	v_mul_lo_u32 v18, v191, s2
	s_add_i32 s2, 0, 0x12000
	v_lshlrev_b32_e32 v19, 2, v190
	v_add3_u32 v194, s2, v18, v19
	v_lshlrev_b32_e32 v18, 3, v52
	v_exp_f32_e32 v84, v20
	v_exp_f32_e32 v85, v21
	v_exp_f32_e32 v86, v22
	v_exp_f32_e32 v87, v23
	v_exp_f32_e32 v88, v24
	v_exp_f32_e32 v89, v25
	v_exp_f32_e32 v66, v34
	v_exp_f32_e32 v67, v35
	v_exp_f32_e32 v68, v36
	v_mov_b32_e32 v69, v37
	v_mov_b32_e32 v70, v38
	v_mov_b32_e32 v71, v39
	v_mov_b32_e32 v72, v40
	v_mov_b32_e32 v73, v41
	v_mov_b32_e32 v74, v42
	v_mov_b32_e32 v75, v43
	v_mov_b32_e32 v76, v44
	v_mov_b32_e32 v77, v45
	v_mov_b32_e32 v78, v46
	v_mov_b32_e32 v79, v47
	v_mov_b32_e32 v80, v48
	v_mov_b32_e32 v81, v49
	v_exp_f32_e32 v90, v26
	v_exp_f32_e32 v91, v27
	v_exp_f32_e32 v92, v28
	v_exp_f32_e32 v93, v29
	v_exp_f32_e32 v94, v30
	v_exp_f32_e32 v95, v31
	v_exp_f32_e32 v96, v32
	v_exp_f32_e32 v97, v33
	v_and_b32_e32 v192, 56, v18
	v_or_b32_e32 v18, s8, v178
	v_mov_b32_e32 v19, s9
	v_lshl_add_u64 v[18:19], v[18:19], 0, v[50:51]
	v_lshl_add_u64 v[18:19], s[6:7], 0, v[18:19]
	s_mov_b64 s[8:9], 0x3580c100
	v_mov_b32_e32 v34, 0
	v_cmp_lt_u32_e64 s[40:41], 31, v190
	v_lshl_add_u32 v196, v195, 2, s2
	v_mul_u32_u24_e32 v197, 0x104, v192
	v_lshl_add_u64 v[162:163], v[18:19], 0, s[8:9]
	v_mov_b32_e32 v35, v34
	v_mov_b32_e32 v36, v34
	v_mov_b32_e32 v37, v34
	v_mov_b32_e32 v38, v34
	v_mov_b32_e32 v39, v34
	v_mov_b32_e32 v40, v34
	v_mov_b32_e32 v41, v34
	v_mov_b32_e32 v42, v34
	v_mov_b32_e32 v43, v34
	v_mov_b32_e32 v44, v34
	v_mov_b32_e32 v45, v34
	v_mov_b32_e32 v46, v34
	v_mov_b32_e32 v47, v34
	v_mov_b32_e32 v48, v34
	v_mov_b32_e32 v49, v34
	v_mov_b32_e32 v18, v34
	v_mov_b32_e32 v19, v34
	v_mov_b32_e32 v20, v34
	v_mov_b32_e32 v21, v34
	v_mov_b32_e32 v22, v34
	v_mov_b32_e32 v23, v34
	v_mov_b32_e32 v24, v34
	v_mov_b32_e32 v25, v34
	v_mov_b32_e32 v26, v34
	v_mov_b32_e32 v27, v34
	v_mov_b32_e32 v28, v34
	v_mov_b32_e32 v29, v34
	v_mov_b32_e32 v30, v34
	v_mov_b32_e32 v31, v34
	v_mov_b32_e32 v32, v34
	v_mov_b32_e32 v33, v34
	v_mov_b32_e32 v50, v34
	v_mov_b32_e32 v51, v34
	v_mov_b32_e32 v52, v34
	v_mov_b32_e32 v53, v34
	v_mov_b32_e32 v54, v34
	v_mov_b32_e32 v55, v34
	v_mov_b32_e32 v56, v34
	v_mov_b32_e32 v57, v34
	v_mov_b32_e32 v58, v34
	v_mov_b32_e32 v59, v34
	v_mov_b32_e32 v60, v34
	v_mov_b32_e32 v61, v34
	v_mov_b32_e32 v62, v34
	v_mov_b32_e32 v63, v34
	v_mov_b32_e32 v64, v34
	v_mov_b32_e32 v65, v34
	v_mov_b64_e32 v[210:211], s[76:77]
	v_mov_b64_e32 v[212:213], s[78:79]
	v_mov_b64_e32 v[214:215], s[80:81]
	v_mov_b64_e32 v[216:217], s[82:83]
	s_branch .LBB0_813

; #define LAS __attribute__((address_space(3)))
; DEV float ex2(float x) { return __builtin_amdgcn_exp2f(x); }
; #define MLA_SB() __builtin_amdgcn_sched_barrier(0)
; #define MLA_PIN(x) asm volatile("" : "+v"(x))
; #define MFMA8(a, b, c) __builtin_amdgcn_mfma_scale_f32_32x32x64_f8f6f4((a), (b), (c), 0, 0, 0, 0x7f7f7f7f, 0, 0x7c7c7c7c)
; #define MFMA8PV(a, b, c) __builtin_amdgcn_mfma_scale_f32_32x32x64_f8f6f4((a), (b), (c), 0, 1, 0, 0x7f7f7f7f, 0, 0x7f7f7f7f)
; DEV unsigned pk_bf8x4(float a, float b, float c, float d, int old = 0) { int w = __builtin_amdgcn_cvt_pk_bf8_f32(a, b, old, false); w = __builtin_amdgcn_cvt_pk_bf8_f32(c, d, w, true); return (unsigned)w; }
; template <int VAR> DEV void mla_step(f32x16& C0, f32x16& C1, f32x16& P0, f32x16& P1, f32x16& o0, f32x16& o1, f32x16& lacc,
;                   const v8i (&qf)[2], const f32x16& cini, LAS char* kp, LAS char* vp, v8i& pw) {
;     v8i kf[2], vf[2];
;     const v8i ones8 = {0x38383838, 0x38383838, 0x38383838, 0x38383838, 0x38383838, 0x38383838, 0x38383838, 0x38383838};
;     kf[0] = mla_kf8(kp, 0, 0); kf[1] = mla_kf8(kp, 1, 0);
;     MLA_SB();
; #pragma unroll
;     for (int g = 0; g < 4; ++g) {
;         const int kb = g & 1, sx = g >> 1;
;         if (kb) C1 = MFMA8(kf[1], qf[sx], sx == 0 ? cini : C1); else C0 = MFMA8(kf[0], qf[sx], sx == 0 ? cini : C0);
;         if (g < 2) kf[kb] = mla_kf8(kp, kb, 1);
;         if (g >= 2) vf[g - 2] = mla_vf8(vp, g - 2);
; #pragma unroll
;         for (int j = 0; j < 2; ++j) { const int w = 2 * g + j, e = 4 * w;
;             if (VAR == 3) pw[w] = __builtin_bit_cast(int, (e < 16) ? P0[e] : P1[e - 16]);
;             else pw[w] = (int)((e < 16) ? pk_bf8x4(P0[e], P0[e + 1], P0[e + 2], P0[e + 3], pw[w]) : pk_bf8x4(P1[e - 16], P1[e - 15], P1[e - 14], P1[e - 13], pw[w])); }
;         if (g == 3) MLA_PIN(pw);
;         MLA_SB();
;     }
; #pragma unroll
;     for (int g = 0; g < 3; ++g) {
;         if (g == 0) o0 = MFMA8PV(vf[0], pw, o0); else if (g == 1) o1 = MFMA8PV(vf[1], pw, o1); else lacc = MFMA8PV(ones8, pw, lacc);
;         const int e0 = (g * 32) / 3, e1 = ((g + 1) * 32) / 3;
; #pragma unroll
;         for (int e = e0; e < e1; ++e) { if (VAR == 2 || VAR == 3) continue; if (e < 16) C0[e] = ex2(C0[e]); else C1[e - 16] = ex2(C1[e - 16]); }
;         if (g < 2) MLA_PIN(C0);
;         if (g > 0) MLA_PIN(C1);
;         MLA_SB();
;     }
; }
.LBB0_812:
	s_mul_i32 s2, s62, 0x6000
	v_add_u32_e32 v172, s2, v200
	ds_read_b128 v[98:101], v172 offset:8192
	ds_read_b128 v[106:109], v172 offset:8704
	ds_read_b128 v[102:105], v172 offset:9216
	ds_read_b128 v[110:113], v172 offset:9728
	v_cvt_pk_bf8_f32 v146, v82, v83
	v_cvt_pk_bf8_f32 v147, v86, v87
	v_exp_f32_e32 v69, v69
	v_exp_f32_e32 v70, v70
	v_exp_f32_e32 v71, v71
	s_waitcnt lgkmcnt(1)
	v_mfma_scale_f32_32x32x64_f8f6f4 v[114:129], v[98:105], v[138:145], v[2:17], v209, v208 op_sel_hi:[0,0,0]
	ds_read_b128 v[154:157], v172 offset:12288
	ds_read_b128 v[158:161], v172 offset:13312
	v_cvt_pk_bf8_f32 v146, v84, v85 op_sel:[0,0,1]
	v_cvt_pk_bf8_f32 v147, v88, v89 op_sel:[0,0,1]
	v_cvt_pk_bf8_f32 v148, v90, v91
	v_cvt_pk_bf8_f32 v149, v94, v95
	ds_read_b128 v[82:85], v172 offset:12800
	ds_read_b128 v[86:89], v172 offset:13824
	v_exp_f32_e32 v72, v72
	v_exp_f32_e32 v73, v73
	s_waitcnt lgkmcnt(4)
	v_mfma_scale_f32_32x32x64_f8f6f4 v[98:113], v[106:113], v[138:145], v[2:17], v209, v208 op_sel_hi:[0,0,0]
	v_cvt_pk_bf8_f32 v148, v92, v93 op_sel:[0,0,1]
	v_cvt_pk_bf8_f32 v149, v96, v97 op_sel:[0,0,1]
	ds_read_b128 v[90:93], v172 offset:16384
	ds_read_b128 v[94:97], v172 offset:17408
	v_exp_f32_e32 v74, v74
	v_exp_f32_e32 v75, v75
	v_exp_f32_e32 v76, v76
	s_waitcnt lgkmcnt(4)
	v_mfma_scale_f32_32x32x64_f8f6f4 v[114:129], v[154:161], v[130:137], v[114:129], v209, v208 op_sel_hi:[0,0,0]
	v_exp_f32_e32 v77, v77
	v_exp_f32_e32 v78, v78
	v_exp_f32_e32 v79, v79
	v_exp_f32_e32 v80, v80
	v_exp_f32_e32 v81, v81
	s_waitcnt lgkmcnt(2)
	v_mfma_scale_f32_32x32x64_f8f6f4 v[98:113], v[82:89], v[130:137], v[98:113], v209, v208 op_sel_hi:[0,0,0]
	v_cvt_pk_bf8_f32 v150, v66, v67
	v_cvt_pk_bf8_f32 v151, v70, v71
	v_cvt_pk_bf8_f32 v150, v68, v69 op_sel:[0,0,1]
	v_cvt_pk_bf8_f32 v151, v72, v73 op_sel:[0,0,1]
	v_cvt_pk_bf8_f32 v152, v74, v75
	v_cvt_pk_bf8_f32 v153, v78, v79
	v_cvt_pk_bf8_f32 v152, v76, v77 op_sel:[0,0,1]
	v_cvt_pk_bf8_f32 v153, v80, v81 op_sel:[0,0,1]
	ds_read_b128 v[66:69], v172 offset:16896
	ds_read_b128 v[70:73], v172 offset:17920
	s_waitcnt lgkmcnt(2)
	v_mfma_scale_f32_32x32x64_f8f6f4 v[50:65], v[90:97], v[146:153], v[50:65], v209, v209 op_sel_hi:[0,0,0] blgp:1
	s_nop 0
	v_exp_f32_e32 v114, v114
	v_exp_f32_e32 v115, v115
	v_exp_f32_e32 v116, v116
	v_exp_f32_e32 v117, v117
	v_exp_f32_e32 v118, v118
	v_exp_f32_e32 v119, v119
	s_waitcnt lgkmcnt(0)
	v_mfma_scale_f32_32x32x64_f8f6f4 v[18:33], v[66:73], v[146:153], v[18:33], v209, v209 op_sel_hi:[0,0,0] blgp:1
	v_exp_f32_e32 v120, v120
	v_exp_f32_e32 v121, v121
	v_exp_f32_e32 v122, v122
	v_exp_f32_e32 v123, v123
	v_exp_f32_e32 v124, v124
	v_exp_f32_e32 v125, v125
	v_mfma_scale_f32_32x32x64_f8f6f4 v[34:49], v[210:217], v[146:153], v[34:49], v209, v209 op_sel_hi:[0,0,0] blgp:1
	v_exp_f32_e32 v126, v126
	v_exp_f32_e32 v127, v127
	v_exp_f32_e32 v128, v128
	v_exp_f32_e32 v129, v129
	v_exp_f32_e32 v98, v98
	v_exp_f32_e32 v99, v99
	v_exp_f32_e32 v100, v100
	s_add_i32 s61, s61, 1
	s_add_i32 s2, s62, 1
	s_cmp_lg_u32 s62, 2
	s_cselect_b32 s62, s2, 0
	s_mul_i32 s64, s62, 0x6000
	s_add_i32 s2, s64, 0x6000
	s_cmp_eq_u32 s62, 2
	s_cselect_b64 s[8:9], -1, 0
	s_waitcnt vmcnt(0)
	s_and_b64 s[20:21], s[8:9], exec
	s_waitcnt lgkmcnt(0)
	s_barrier
	s_cselect_b32 s2, 0, s2
	s_add_i32 s2, s2, s60
	s_mov_b32 s3, m0
	s_mov_b32 m0, s2
	v_add_u32_e32 v173, s64, v200
	ds_read_b128 v[66:69], v173
	ds_read_b128 v[74:77], v173 offset:512
	ds_read_b128 v[70:73], v173 offset:1024
	ds_read_b128 v[78:81], v173 offset:1536
	v_cvt_pk_bf8_f32 v146, v114, v115
	v_cvt_pk_bf8_f32 v147, v118, v119
	v_exp_f32_e32 v101, v101
	v_exp_f32_e32 v102, v102
	v_exp_f32_e32 v103, v103
	s_waitcnt lgkmcnt(1)
	v_mfma_scale_f32_32x32x64_f8f6f4 v[82:97], v[66:73], v[138:145], v[2:17], v209, v208 op_sel_hi:[0,0,0]
	global_load_lds_dwordx4 v[162:163], off
	ds_read_b128 v[164:167], v173 offset:4096
	ds_read_b128 v[168:171], v173 offset:5120
	v_cvt_pk_bf8_f32 v146, v116, v117 op_sel:[0,0,1]
	v_cvt_pk_bf8_f32 v147, v120, v121 op_sel:[0,0,1]
	v_cvt_pk_bf8_f32 v148, v122, v123
	v_cvt_pk_bf8_f32 v149, v126, v127
	ds_read_b128 v[114:117], v173 offset:4608
	ds_read_b128 v[118:121], v173 offset:5632
	v_exp_f32_e32 v104, v104
	v_exp_f32_e32 v105, v105
	s_waitcnt lgkmcnt(4)
	v_mfma_scale_f32_32x32x64_f8f6f4 v[66:81], v[74:81], v[138:145], v[2:17], v209, v208 op_sel_hi:[0,0,0]
	global_load_lds_dwordx4 v[162:163], off offset:1024
	v_cvt_pk_bf8_f32 v148, v124, v125 op_sel:[0,0,1]
	v_cvt_pk_bf8_f32 v149, v128, v129 op_sel:[0,0,1]
	ds_read_b128 v[122:125], v172 offset:20480
	ds_read_b128 v[126:129], v172 offset:21504
	v_exp_f32_e32 v106, v106
	v_exp_f32_e32 v107, v107
	v_exp_f32_e32 v108, v108
	s_waitcnt lgkmcnt(4)
	v_mfma_scale_f32_32x32x64_f8f6f4 v[82:97], v[164:171], v[130:137], v[82:97], v209, v208 op_sel_hi:[0,0,0]
	global_load_lds_dwordx4 v[162:163], off offset:2048
	s_mov_b32 m0, s3
	v_exp_f32_e32 v109, v109
	v_exp_f32_e32 v110, v110
	v_exp_f32_e32 v111, v111
	v_exp_f32_e32 v112, v112
	v_exp_f32_e32 v113, v113
	s_waitcnt lgkmcnt(2)
	v_mfma_scale_f32_32x32x64_f8f6f4 v[66:81], v[114:121], v[130:137], v[66:81], v209, v208 op_sel_hi:[0,0,0]
	v_cvt_pk_bf8_f32 v150, v98, v99
	v_cvt_pk_bf8_f32 v151, v102, v103
	v_cvt_pk_bf8_f32 v150, v100, v101 op_sel:[0,0,1]
	v_cvt_pk_bf8_f32 v151, v104, v105 op_sel:[0,0,1]
	v_cvt_pk_bf8_f32 v152, v106, v107
	v_cvt_pk_bf8_f32 v153, v110, v111
	v_cvt_pk_bf8_f32 v152, v108, v109 op_sel:[0,0,1]
	v_cvt_pk_bf8_f32 v153, v112, v113 op_sel:[0,0,1]
	ds_read_b128 v[98:101], v172 offset:20992
	ds_read_b128 v[102:105], v172 offset:22016
	s_waitcnt lgkmcnt(2)
	v_mfma_scale_f32_32x32x64_f8f6f4 v[50:65], v[122:129], v[146:153], v[50:65], v209, v209 op_sel_hi:[0,0,0] blgp:1
	s_nop 0
	v_exp_f32_e32 v82, v82
	v_exp_f32_e32 v83, v83
	v_exp_f32_e32 v84, v84
	v_exp_f32_e32 v85, v85
	v_exp_f32_e32 v86, v86
	v_exp_f32_e32 v87, v87
	s_waitcnt lgkmcnt(0)
	v_mfma_scale_f32_32x32x64_f8f6f4 v[18:33], v[98:105], v[146:153], v[18:33], v209, v209 op_sel_hi:[0,0,0] blgp:1
	v_exp_f32_e32 v88, v88
	v_exp_f32_e32 v89, v89
	v_exp_f32_e32 v90, v90
	v_exp_f32_e32 v91, v91
	v_exp_f32_e32 v92, v92
	v_exp_f32_e32 v93, v93
	v_mfma_scale_f32_32x32x64_f8f6f4 v[34:49], v[210:217], v[146:153], v[34:49], v209, v209 op_sel_hi:[0,0,0] blgp:1
	v_exp_f32_e32 v94, v94
	v_exp_f32_e32 v95, v95
	v_exp_f32_e32 v96, v96
	v_exp_f32_e32 v97, v97
	v_exp_f32_e32 v66, v66
	v_exp_f32_e32 v67, v67
	v_exp_f32_e32 v68, v68
	s_mov_b64 s[20:21], 0x6000
	s_cmpk_lg_i32 s61, 0x80
	v_lshl_add_u64 v[162:163], v[162:163], 0, s[20:21]
	s_cbranch_scc0 .LBB0_835
